# each kernel warms the next kernel's code in its XCD L2 (sort->first, first->FF, FF->FT, FT->final)
# speedup vs baseline: 1.0451x; 1.0112x over previous
.LBB0_6:
	s_or_b64 exec, exec, s[4:5]
	s_waitcnt lgkmcnt(0)
	s_barrier
	ds_read_b32 v19, v29
	v_lshl_add_u32 v26, v26, s8, v27
	ds_read_b32 v27, v30
	ds_read_b32 v28, v28
	ds_read_b32 v25, v25
	s_waitcnt vmcnt(3)
	v_cmp_eq_u32_e32 vcc, 0, v17
	s_mov_b64 s[4:5], -1
	s_waitcnt lgkmcnt(3)
	v_add_lshl_u32 v19, v26, v19, 2
	ds_write2st64_b32 v19, v8, v9 offset1:64
	v_bfrev_b32_e32 v8, 1
	v_cndmask_b32_e32 v8, 0, v8, vcc
	v_or_b32_e32 v8, v8, v0
	ds_write_b32 v19, v8 offset:32768
	v_lshl_add_u32 v8, v20, s8, v21
	s_waitcnt lgkmcnt(4)
	v_add_lshl_u32 v8, v8, v27, 2
	ds_write2st64_b32 v8, v4, v5 offset1:64
	v_mov_b32_e32 v4, 0x400
	v_mov_b32_e32 v5, 0x80000400
	s_waitcnt vmcnt(2)
	v_cmp_eq_u32_e32 vcc, 0, v16
	s_nop 1
	v_cndmask_b32_e32 v4, v4, v5, vcc
	v_or_b32_e32 v4, v4, v0
	ds_write_b32 v8, v4 offset:32768
	v_lshl_add_u32 v4, v22, s8, v23
	s_waitcnt lgkmcnt(5)
	v_add_lshl_u32 v4, v4, v28, 2
	ds_write2st64_b32 v4, v6, v7 offset1:64
	v_mov_b32_e32 v5, 0x800
	v_mov_b32_e32 v6, 0x80000800
	s_waitcnt vmcnt(1)
	v_cmp_eq_u32_e32 vcc, 0, v15
	s_nop 1
	v_cndmask_b32_e32 v5, v5, v6, vcc
	v_or_b32_e32 v5, v5, v0
	ds_write_b32 v4, v5 offset:32768
	v_lshl_add_u32 v4, v24, s8, v18
	s_waitcnt lgkmcnt(6)
	v_add_lshl_u32 v4, v4, v25, 2
	ds_write2st64_b32 v4, v2, v3 offset1:64
	v_mov_b32_e32 v2, 0xc00
	v_mov_b32_e32 v3, 0x80000c00
	s_waitcnt vmcnt(0)
	v_cmp_eq_u32_e32 vcc, 0, v14
	s_nop 1
	v_cndmask_b32_e32 v2, v2, v3, vcc
	v_or_b32_e32 v2, v2, v0
	ds_write_b32 v4, v2 offset:32768
	s_waitcnt lgkmcnt(0)
	s_barrier
	s_getpc_b64 s[30:31]
	s_add_u32 s30, s30, 0x24d8
	s_addc_u32 s31, s31, 0
	v_lshlrev_b32_e32 v40, 6, v0
	v_min_u32_e32 v40, 0x2d00, v40
	global_load_dword v40, v40, s[30:31]
	ds_read_b32 v14, v11 offset:32768
	s_load_dwordx2 s[18:19], s[0:1], 0x60
	s_load_dwordx8 s[8:15], s[0:1], 0x40
	ds_read2st64_b32 v[4:5], v11 offset1:64
	v_or_b32_e32 v2, s16, v0
	v_mov_b32_e32 v3, 0
	s_waitcnt lgkmcnt(0)
	v_and_b32_e32 v15, 0x7fffffff, v14
	s_and_b64 vcc, exec, s[2:3]
	v_lshlrev_b64 v[6:7], 2, v[2:3]
	s_cbranch_vccz .LBB0_8
	v_lshl_add_u64 v[8:9], s[10:11], 0, v[6:7]
	global_store_dword v[8:9], v4, off
	v_lshl_add_u64 v[8:9], s[12:13], 0, v[6:7]
	global_store_dword v[8:9], v5, off
	v_lshl_add_u64 v[8:9], s[14:15], 0, v[6:7]
	global_store_dword v[8:9], v15, off
	s_mov_b64 s[4:5], 0

	.amdhsa_kernel _Z6k_sortPKfS0_PKiS2_PiP15HIP_vector_typeIfLj4EEPfS7_S3_S7_S7_S3_S3_S6_S6_
		.amdhsa_group_segment_fixed_size 67584
		.amdhsa_private_segment_fixed_size 0
		.amdhsa_kernarg_size 120
		.amdhsa_user_sgpr_count 2
		.amdhsa_user_sgpr_dispatch_ptr 0
		.amdhsa_user_sgpr_queue_ptr 0
		.amdhsa_user_sgpr_kernarg_segment_ptr 1
		.amdhsa_user_sgpr_dispatch_id 0
		.amdhsa_user_sgpr_kernarg_preload_length 0
		.amdhsa_user_sgpr_kernarg_preload_offset 0
		.amdhsa_user_sgpr_private_segment_size 0
		.amdhsa_uses_dynamic_stack 0
		.amdhsa_enable_private_segment 0
		.amdhsa_system_sgpr_workgroup_id_x 1
		.amdhsa_system_sgpr_workgroup_id_y 0
		.amdhsa_system_sgpr_workgroup_id_z 0
		.amdhsa_system_sgpr_workgroup_info 0
		.amdhsa_system_vgpr_workitem_id 0
		.amdhsa_next_free_vgpr 48
		.amdhsa_next_free_sgpr 36
		.amdhsa_accum_offset 48
		.amdhsa_reserve_vcc 1
		.amdhsa_float_round_mode_32 0
		.amdhsa_float_round_mode_16_64 0
		.amdhsa_float_denorm_mode_32 3
		.amdhsa_float_denorm_mode_16_64 3
		.amdhsa_dx10_clamp 1
		.amdhsa_ieee_mode 1
		.amdhsa_fp16_overflow 0
		.amdhsa_tg_split 0
		.amdhsa_exception_fp_ieee_invalid_op 0
		.amdhsa_exception_fp_denorm_src 0
		.amdhsa_exception_fp_ieee_div_zero 0
		.amdhsa_exception_fp_ieee_overflow 0
		.amdhsa_exception_fp_ieee_underflow 0
		.amdhsa_exception_fp_ieee_inexact 0
		.amdhsa_exception_int_div_zero 0
	.end_amdhsa_kernel

.LBB2_99:
	s_or_b64 exec, exec, s[22:23]
	s_lshr_b32 s66, s33, 3
	s_or_b32 s66, s66, s26
	s_add_i32 s66, s66, s27
	s_mov_b32 s67, 0
	s_lshl_b64 s[66:67], s[66:67], 10
	s_add_u32 s66, s30, s66
	s_addc_u32 s67, s31, s67
	v_lshlrev_b32_e32 v208, 4, v44
	s_waitcnt vmcnt(0)
	v_cvt_pk_f16_f32 v210, v200, v201
	v_cvt_pk_f16_f32 v211, v202, v203
	v_cvt_pk_f16_f32 v212, v204, v205
	v_cvt_pk_f16_f32 v213, v206, v207
	global_store_dwordx4 v208, v[210:213], s[66:67]
	s_getpc_b64 s[66:67]
.Lfirst_pc:
	s_add_u32 s66, s66, (.Lfirst_code_end-.Lfirst_pc)&4294967295
	s_addc_u32 s67, s67, 0
	s_lshl_b32 s68, s27, 12
	v_lshl_or_b32 v214, v44, 6, s68
	v_min_u32_e32 v214, 0x3300, v214
	global_load_dword v214, v214, s[66:67]
	s_andn2_b64 vcc, exec, s[0:1]
	s_waitcnt lgkmcnt(0)
	s_barrier
	s_cbranch_vccnz .LBB2_117
	v_lshlrev_b32_e32 v0, 3, v1
	v_add_u32_e32 v0, 0x7000, v0
	ds_read2_b64 v[12:15], v0 offset0:196 offset1:198
	ds_read2_b64 v[8:11], v0 offset0:200 offset1:202
	ds_read2_b64 v[4:7], v0 offset0:204 offset1:206
	ds_read2_b64 v[0:3], v0 offset0:208 offset1:210
	v_mov_b32_e32 v21, 0
	ds_read_b32 v36, v21 offset:30368
	s_cmp_lt_i32 s39, 4
	s_mov_b64 s[0:1], 0
	s_cbranch_scc1 .LBB2_118
	s_cmp_gt_i32 s39, 4
	s_cbranch_scc0 .LBB2_119
	s_cmp_gt_i32 s39, 5
	s_cbranch_scc0 .LBB2_129
	s_mov_b64 s[8:9], 0
	s_cmp_eq_u32 s39, 6
	s_mov_b64 s[14:15], 0
	s_cbranch_scc0 .LBB2_107
	v_mov_b32_e32 v37, 0
	s_waitcnt lgkmcnt(4)
	v_dot2c_f32_f16_e32 v37, v20, v12
	v_mov_b32_e32 v20, 0
	v_dot2c_f32_f16_e32 v20, v49, v13
	v_dot2c_f32_f16_e32 v37, v54, v14
	v_dot2c_f32_f16_e32 v20, v57, v15
	s_waitcnt lgkmcnt(3)
	v_dot2c_f32_f16_e32 v37, v61, v8
	v_dot2c_f32_f16_e32 v20, v64, v9
	v_dot2c_f32_f16_e32 v37, v67, v10
	v_dot2c_f32_f16_e32 v20, v69, v11
	s_waitcnt lgkmcnt(2)
	v_dot2c_f32_f16_e32 v37, v75, v4
	v_dot2c_f32_f16_e32 v20, v79, v5
	v_dot2c_f32_f16_e32 v37, v85, v6
	v_dot2c_f32_f16_e32 v20, v88, v7
	s_waitcnt lgkmcnt(1)
	v_dot2c_f32_f16_e32 v37, v91, v0
	v_dot2c_f32_f16_e32 v20, v94, v1
	v_dot2c_f32_f16_e32 v37, v97, v2
	v_dot2c_f32_f16_e32 v20, v98, v3
	s_and_b64 vcc, s[18:19], s[12:13]
	v_cndmask_b32_e32 v35, -1, v35, vcc
	v_mov_b32_e32 v21, 0
	v_add_f32_e32 v20, v37, v20
	v_mov_b32_e32 v37, v20
	s_nop 1
	v_permlane32_swap_b32_e32 v20, v37
	v_cmp_lt_i32_e32 vcc, -1, v35
	s_and_saveexec_b64 s[12:13], vcc
	s_cbranch_execz .LBB2_106
	v_add_f32_e32 v20, v20, v37
	s_waitcnt lgkmcnt(0)
	v_mul_f32_e32 v37, v36, v20
	v_add_u32_e32 v20, s58, v35
	v_lshl_add_u64 v[20:21], v[20:21], 2, s[34:35]
	global_atomic_add_f32 v[20:21], v37, off

.LBB2_154:
	v_pk_add_f16 v21, v18, v1
	v_pk_add_f16 v36, v22, v2
	v_pk_add_f16 v37, v24, v3
	v_pk_add_f16 v38, v25, v4
	v_pk_add_f16 v39, v26, v5
	v_pk_add_f16 v40, v28, v6
	v_pk_add_f16 v41, v29, v7
	v_pk_add_f16 v42, v30, v8
	v_pk_add_f16 v43, v32, v9
	v_pk_add_f16 v115, v33, v10
	v_pk_add_f16 v131, v34, v11
	v_pk_add_f16 v132, v47, v12
	v_pk_add_f16 v133, v51, v13
	v_pk_add_f16 v134, v52, v14
	v_pk_add_f16 v135, v56, v15
	v_pk_add_f16 v136, v59, v16
	s_mov_b64 s[16:17], -1
	s_mov_b64 s[22:23], 0
	s_and_b64 vcc, exec, s[16:17]
	s_mov_b64 s[16:17], 0
	s_cbranch_vccz .LBB2_68
	s_branch .LBB2_67
	.p2align	8
.Lfirst_code_end:
	.section	.rodata,"a",@progbits
	.p2align	6, 0x0
	.amdhsa_kernel _Z6k_iterILb1ELb0EEvPKfS1_PKiPK15HIP_vector_typeIfLj4EES7_S1_S1_S3_S1_PfS8_S1_S3_PDF16_PS5_SA_PiSA_SB_
		.amdhsa_group_segment_fixed_size 30384
		.amdhsa_private_segment_fixed_size 0
		.amdhsa_kernarg_size 152
		.amdhsa_user_sgpr_count 2
		.amdhsa_user_sgpr_dispatch_ptr 0
		.amdhsa_user_sgpr_queue_ptr 0
		.amdhsa_user_sgpr_kernarg_segment_ptr 1
		.amdhsa_user_sgpr_dispatch_id 0
		.amdhsa_user_sgpr_kernarg_preload_length 0
		.amdhsa_user_sgpr_kernarg_preload_offset 0
		.amdhsa_user_sgpr_private_segment_size 0
		.amdhsa_uses_dynamic_stack 0
		.amdhsa_enable_private_segment 0
		.amdhsa_system_sgpr_workgroup_id_x 1
		.amdhsa_system_sgpr_workgroup_id_y 0
		.amdhsa_system_sgpr_workgroup_id_z 0
		.amdhsa_system_sgpr_workgroup_info 0
		.amdhsa_system_vgpr_workitem_id 0
		.amdhsa_next_free_vgpr 216
		.amdhsa_next_free_sgpr 96
		.amdhsa_accum_offset 216
		.amdhsa_reserve_vcc 1
		.amdhsa_float_round_mode_32 0
		.amdhsa_float_round_mode_16_64 0
		.amdhsa_float_denorm_mode_32 3
		.amdhsa_float_denorm_mode_16_64 3
		.amdhsa_dx10_clamp 1
		.amdhsa_ieee_mode 1
		.amdhsa_fp16_overflow 0
		.amdhsa_tg_split 0
		.amdhsa_exception_fp_ieee_invalid_op 0
		.amdhsa_exception_fp_denorm_src 0
		.amdhsa_exception_fp_ieee_div_zero 0
		.amdhsa_exception_fp_ieee_overflow 0
		.amdhsa_exception_fp_ieee_underflow 0
		.amdhsa_exception_fp_ieee_inexact 0
		.amdhsa_exception_int_div_zero 0
	.end_amdhsa_kernel

.LBB4_39:
	s_waitcnt vmcnt(5)
	v_rcp_f32_e32 v2, v133
	s_waitcnt vmcnt(4)
	v_rcp_f32_e32 v3, v132
	s_waitcnt vmcnt(3)
	v_rcp_f32_e32 v4, v131
	v_cmp_lt_f32_e32 vcc, 0, v133
	s_waitcnt vmcnt(2)
	v_rcp_f32_e32 v5, v130
	s_waitcnt vmcnt(1)
	v_rcp_f32_e32 v6, v129
	v_cndmask_b32_e32 v2, 0, v2, vcc
	v_cmp_lt_f32_e32 vcc, 0, v132
	s_waitcnt vmcnt(0)
	v_rcp_f32_e32 v7, v128
	s_getpc_b64 s[36:37]
	s_sub_u32 s36, s36, 0x912c
	s_subb_u32 s37, s37, 0
	v_lshlrev_b32_e32 v183, 6, v0
	v_min_u32_e32 v183, 0x1980, v183
	global_load_dword v183, v183, s[36:37]
	s_mov_b32 s4, 0x42c80000
	v_cndmask_b32_e32 v3, 0, v3, vcc
	v_cmp_lt_f32_e32 vcc, 0, v131
	v_cmp_ngt_f32_e64 s[2:3], s4, v3
	s_mov_b64 s[6:7], 0
	v_cndmask_b32_e32 v4, 0, v4, vcc
	v_cmp_lt_f32_e32 vcc, 0, v130
	s_nop 1
	v_cndmask_b32_e32 v5, 0, v5, vcc
	v_cmp_lt_f32_e32 vcc, 0, v129
	s_nop 1
	v_cndmask_b32_e32 v6, 0, v6, vcc
	v_cmp_lt_f32_e32 vcc, 0, v128
	s_nop 1
	v_cndmask_b32_e32 v7, 0, v7, vcc
	v_cmp_ngt_f32_e32 vcc, s4, v2
	s_or_b64 s[2:3], vcc, s[2:3]
	v_cmp_ngt_f32_e32 vcc, s4, v4
	s_or_b64 s[2:3], s[2:3], vcc
	v_cmp_ngt_f32_e32 vcc, s4, v5
	s_or_b64 s[2:3], s[2:3], vcc
	v_cmp_ngt_f32_e32 vcc, s4, v6
	s_or_b64 s[2:3], s[2:3], vcc
	v_cmp_ngt_f32_e32 vcc, s4, v7
	s_or_b64 s[2:3], s[2:3], vcc
	v_cndmask_b32_e64 v8, 0, 1, s[2:3]
	v_cmp_ne_u32_e32 vcc, 0, v8
	s_cmp_eq_u64 vcc, 0
	s_cselect_b64 s[2:3], -1, 0
	v_cndmask_b32_e64 v8, 0, 1, s[2:3]
	s_nop 0
	v_readfirstlane_b32 s2, v8
	s_bitcmp0_b32 s2, 0
	s_cbranch_scc0 .LBB4_45
	s_cmp_lt_i32 s28, 4
	s_cbranch_scc1 .LBB4_46
	s_cmp_gt_i32 s28, 4
	s_cbranch_scc0 .LBB4_47
	s_mov_b64 s[4:5], -1
	v_mov_b32_e32 v8, 0
	s_cmp_gt_i32 s28, 5
	v_mov_b32_e32 v167, 0
	v_mov_b32_e32 v166, 0
	v_mov_b32_e32 v165, 0
	v_mov_b32_e32 v164, 0
	v_mov_b32_e32 v162, 0
	v_mov_b32_e32 v160, 0
	v_mov_b32_e32 v159, 0
	v_mov_b32_e32 v157, 0
	v_mov_b32_e32 v151, 0
	v_mov_b32_e32 v149, 0
	v_mov_b32_e32 v147, 0
	v_mov_b32_e32 v146, 0
	v_mov_b32_e32 v144, 0
	v_mov_b32_e32 v143, 0
	v_mov_b32_e32 v152, 0
	v_mov_b32_e32 v153, 0
	v_mov_b32_e32 v154, 0
	v_mov_b32_e32 v155, 0
	v_mov_b32_e32 v156, 0
	v_mov_b32_e32 v158, 0
	v_mov_b32_e32 v161, 0
	v_mov_b32_e32 v163, 0
	v_mov_b32_e32 v168, 0
	v_mov_b32_e32 v169, 0
	v_mov_b32_e32 v170, 0
	v_mov_b32_e32 v171, 0
	v_mov_b32_e32 v172, 0
	v_mov_b32_e32 v173, 0
	v_mov_b32_e32 v174, 0
	v_mov_b32_e32 v145, 0
	v_mov_b32_e32 v148, 0
	v_mov_b32_e32 v150, 0
	s_cbranch_scc0 .LBB4_50
	s_cmp_eq_u32 s28, 6
	s_cbranch_scc0 .LBB4_49
	v_mov_b32_e32 v145, 0
	v_mov_b32_e32 v148, 0
	v_mov_b32_e32 v150, 0
	v_mov_b32_e32 v143, 0
	v_mov_b32_e32 v144, 0
	v_mov_b32_e32 v146, 0
	v_mov_b32_e32 v147, 0
	v_mov_b32_e32 v149, 0
	v_mov_b32_e32 v151, 0
	v_mov_b32_e32 v152, 0
	v_mov_b32_e32 v153, 0
	v_mov_b32_e32 v154, 0
	v_mov_b32_e32 v155, 0
	v_mov_b32_e32 v156, 0
	v_mov_b32_e32 v158, 0
	v_mov_b32_e32 v161, 0
	v_mov_b32_e32 v163, 0
	v_mov_b32_e32 v157, 0
	v_mov_b32_e32 v159, 0
	v_mov_b32_e32 v160, 0
	v_mov_b32_e32 v162, 0
	v_mov_b32_e32 v164, 0
	v_mov_b32_e32 v165, 0
	v_mov_b32_e32 v166, 0
	v_mov_b32_e32 v167, 0
	v_mov_b32_e32 v168, 0
	v_mov_b32_e32 v169, 0
	v_mov_b32_e32 v170, 0
	v_mov_b32_e32 v171, 0
	v_mov_b32_e32 v172, 0
	v_mov_b32_e32 v173, 0
	v_mov_b32_e32 v174, 0
	v_fma_mix_f32 v148, v43, v7, v148 op_sel_hi:[1,0,0]
	v_fma_mix_f32 v150, v45, v7, v150 op_sel_hi:[1,0,0]
	v_fma_mix_f32 v143, v50, v7, v143 op_sel_hi:[1,0,0]
	v_fma_mix_f32 v144, v54, v7, v144 op_sel_hi:[1,0,0]
	v_fma_mix_f32 v146, v58, v7, v146 op_sel_hi:[1,0,0]
	v_fma_mix_f32 v147, v61, v7, v147 op_sel_hi:[1,0,0]
	v_fma_mix_f32 v149, v64, v7, v149 op_sel_hi:[1,0,0]
	v_fma_mix_f32 v151, v66, v7, v151 op_sel_hi:[1,0,0]
	v_fma_mix_f32 v152, v43, v7, v152 op_sel:[1,0,0] op_sel_hi:[1,0,0]
	v_fma_mix_f32 v153, v45, v7, v153 op_sel:[1,0,0] op_sel_hi:[1,0,0]
	v_fma_mix_f32 v154, v50, v7, v154 op_sel:[1,0,0] op_sel_hi:[1,0,0]
	v_fma_mix_f32 v155, v54, v7, v155 op_sel:[1,0,0] op_sel_hi:[1,0,0]
	v_fma_mix_f32 v156, v58, v7, v156 op_sel:[1,0,0] op_sel_hi:[1,0,0]
	v_fma_mix_f32 v158, v61, v7, v158 op_sel:[1,0,0] op_sel_hi:[1,0,0]
	v_fma_mix_f32 v161, v64, v7, v161 op_sel:[1,0,0] op_sel_hi:[1,0,0]
	v_fma_mix_f32 v163, v66, v7, v163 op_sel:[1,0,0] op_sel_hi:[1,0,0]
	v_fma_mix_f32 v157, v72, v7, v157 op_sel_hi:[1,0,0]
	v_fma_mix_f32 v159, v76, v7, v159 op_sel_hi:[1,0,0]
	v_fma_mix_f32 v160, v83, v7, v160 op_sel_hi:[1,0,0]
	v_fma_mix_f32 v162, v85, v7, v162 op_sel_hi:[1,0,0]
	v_fma_mix_f32 v164, v89, v7, v164 op_sel_hi:[1,0,0]
	v_fma_mix_f32 v165, v92, v7, v165 op_sel_hi:[1,0,0]
	v_fma_mix_f32 v166, v95, v7, v166 op_sel_hi:[1,0,0]
	v_fma_mix_f32 v167, v96, v7, v167 op_sel_hi:[1,0,0]
	v_fma_mix_f32 v168, v72, v7, v168 op_sel:[1,0,0] op_sel_hi:[1,0,0]
	v_fma_mix_f32 v169, v76, v7, v169 op_sel:[1,0,0] op_sel_hi:[1,0,0]
	v_fma_mix_f32 v170, v83, v7, v170 op_sel:[1,0,0] op_sel_hi:[1,0,0]
	v_fma_mix_f32 v171, v85, v7, v171 op_sel:[1,0,0] op_sel_hi:[1,0,0]
	v_fma_mix_f32 v172, v89, v7, v172 op_sel:[1,0,0] op_sel_hi:[1,0,0]
	v_fma_mix_f32 v173, v92, v7, v173 op_sel:[1,0,0] op_sel_hi:[1,0,0]
	v_fma_mix_f32 v174, v95, v7, v174 op_sel:[1,0,0] op_sel_hi:[1,0,0]
	v_fma_mix_f32 v145, v96, v7, v145 op_sel:[1,0,0] op_sel_hi:[1,0,0]
	s_branch .LBB4_50

	.amdhsa_kernel _Z6k_iterILb0ELb1EEvPKfS1_PKiPK15HIP_vector_typeIfLj4EES7_S1_S1_S3_S1_PfS8_S1_S3_PDF16_PS5_SA_PiSA_SB_
		.amdhsa_group_segment_fixed_size 5808
		.amdhsa_private_segment_fixed_size 0
		.amdhsa_kernarg_size 152
		.amdhsa_user_sgpr_count 2
		.amdhsa_user_sgpr_dispatch_ptr 0
		.amdhsa_user_sgpr_queue_ptr 0
		.amdhsa_user_sgpr_kernarg_segment_ptr 1
		.amdhsa_user_sgpr_dispatch_id 0
		.amdhsa_user_sgpr_kernarg_preload_length 0
		.amdhsa_user_sgpr_kernarg_preload_offset 0
		.amdhsa_user_sgpr_private_segment_size 0
		.amdhsa_uses_dynamic_stack 0
		.amdhsa_enable_private_segment 0
		.amdhsa_system_sgpr_workgroup_id_x 1
		.amdhsa_system_sgpr_workgroup_id_y 0
		.amdhsa_system_sgpr_workgroup_id_z 0
		.amdhsa_system_sgpr_workgroup_info 0
		.amdhsa_system_vgpr_workitem_id 0
		.amdhsa_next_free_vgpr 184
		.amdhsa_next_free_sgpr 40
		.amdhsa_accum_offset 184
		.amdhsa_reserve_vcc 1
		.amdhsa_float_round_mode_32 0
		.amdhsa_float_round_mode_16_64 0
		.amdhsa_float_denorm_mode_32 3
		.amdhsa_float_denorm_mode_16_64 3
		.amdhsa_dx10_clamp 1
		.amdhsa_ieee_mode 1
		.amdhsa_fp16_overflow 0
		.amdhsa_tg_split 0
		.amdhsa_exception_fp_ieee_invalid_op 0
		.amdhsa_exception_fp_denorm_src 0
		.amdhsa_exception_fp_ieee_div_zero 0
		.amdhsa_exception_fp_ieee_overflow 0
		.amdhsa_exception_fp_ieee_underflow 0
		.amdhsa_exception_fp_ieee_inexact 0
		.amdhsa_exception_int_div_zero 0
	.end_amdhsa_kernel

amdhsa.kernels:
  - .agpr_count:     0
    .args:
      - .actual_access:  read_only
        .address_space:  global
        .offset:         0
        .size:           8
        .value_kind:     global_buffer
      - .actual_access:  read_only
        .address_space:  global
        .offset:         8
        .size:           8
        .value_kind:     global_buffer
      - .actual_access:  read_only
        .address_space:  global
        .offset:         16
        .size:           8
        .value_kind:     global_buffer
      - .actual_access:  read_only
        .address_space:  global
        .offset:         24
        .size:           8
        .value_kind:     global_buffer
      - .actual_access:  write_only
        .address_space:  global
        .offset:         32
        .size:           8
        .value_kind:     global_buffer
      - .actual_access:  write_only
        .address_space:  global
        .offset:         40
        .size:           8
        .value_kind:     global_buffer
      - .actual_access:  write_only
        .address_space:  global
        .offset:         48
        .size:           8
        .value_kind:     global_buffer
      - .actual_access:  write_only
        .address_space:  global
        .offset:         56
        .size:           8
        .value_kind:     global_buffer
      - .actual_access:  write_only
        .address_space:  global
        .offset:         64
        .size:           8
        .value_kind:     global_buffer
      - .actual_access:  write_only
        .address_space:  global
        .offset:         72
        .size:           8
        .value_kind:     global_buffer
      - .actual_access:  write_only
        .address_space:  global
        .offset:         80
        .size:           8
        .value_kind:     global_buffer
      - .actual_access:  write_only
        .address_space:  global
        .offset:         88
        .size:           8
        .value_kind:     global_buffer
      - .actual_access:  write_only
        .address_space:  global
        .offset:         96
        .size:           8
        .value_kind:     global_buffer
      - .actual_access:  write_only
        .address_space:  global
        .offset:         104
        .size:           8
        .value_kind:     global_buffer
      - .actual_access:  write_only
        .address_space:  global
        .offset:         112
        .size:           8
        .value_kind:     global_buffer
    .group_segment_fixed_size: 67584
    .kernarg_segment_align: 8
    .kernarg_segment_size: 120
    .language:       OpenCL C
    .language_version:
      - 2
      - 0
    .max_flat_workgroup_size: 1024
    .name:           _Z6k_sortPKfS0_PKiS2_PiP15HIP_vector_typeIfLj4EEPfS7_S3_S7_S7_S3_S3_S6_S6_
    .private_segment_fixed_size: 0
    .sgpr_count:     42
    .sgpr_spill_count: 0
    .symbol:         _Z6k_sortPKfS0_PKiS2_PiP15HIP_vector_typeIfLj4EEPfS7_S3_S7_S7_S3_S3_S6_S6_.kd
    .uniform_work_group_size: 1
    .uses_dynamic_stack: false
    .vgpr_count:     48
    .vgpr_spill_count: 0
    .wavefront_size: 64
  - .agpr_count:     0
    .args:
      - .actual_access:  read_only
        .address_space:  global
        .offset:         0
        .size:           8
        .value_kind:     global_buffer
      - .actual_access:  read_only
        .address_space:  global
        .offset:         8
        .size:           8
        .value_kind:     global_buffer
      - .actual_access:  read_only
        .address_space:  global
        .offset:         16
        .size:           8
        .value_kind:     global_buffer
      - .actual_access:  read_only
        .address_space:  global
        .offset:         24
        .size:           8
        .value_kind:     global_buffer
      - .actual_access:  read_only
        .address_space:  global
        .offset:         32
        .size:           8
        .value_kind:     global_buffer
      - .actual_access:  read_only
        .address_space:  global
        .offset:         40
        .size:           8
        .value_kind:     global_buffer
      - .actual_access:  read_only
        .address_space:  global
        .offset:         48
        .size:           8
        .value_kind:     global_buffer
      - .actual_access:  write_only
        .address_space:  global
        .offset:         56
        .size:           8
        .value_kind:     global_buffer
    .group_segment_fixed_size: 145952
    .kernarg_segment_align: 8
    .kernarg_segment_size: 64
    .language:       OpenCL C
    .language_version:
      - 2
      - 0
    .max_flat_workgroup_size: 512
    .name:           _Z7k_finalPK15HIP_vector_typeIfLj4EES2_PKiS4_PKfS6_PKDF16_Pf
    .private_segment_fixed_size: 0
    .sgpr_count:     34
    .sgpr_spill_count: 0
    .symbol:         _Z7k_finalPK15HIP_vector_typeIfLj4EES2_PKiS4_PKfS6_PKDF16_Pf.kd
    .uniform_work_group_size: 1
    .uses_dynamic_stack: false
    .vgpr_count:     177
    .vgpr_spill_count: 0
    .wavefront_size: 64
  - .agpr_count:     0
    .args:
      - .actual_access:  read_only
        .address_space:  global
        .offset:         0
        .size:           8
        .value_kind:     global_buffer
      - .actual_access:  read_only
        .address_space:  global
        .offset:         8
        .size:           8
        .value_kind:     global_buffer
      - .actual_access:  read_only
        .address_space:  global
        .offset:         16
        .size:           8
        .value_kind:     global_buffer
      - .actual_access:  read_only
        .address_space:  global
        .offset:         24
        .size:           8
        .value_kind:     global_buffer
      - .actual_access:  read_only
        .address_space:  global
        .offset:         32
        .size:           8
        .value_kind:     global_buffer
      - .actual_access:  read_only
        .address_space:  global
        .offset:         40
        .size:           8
        .value_kind:     global_buffer
      - .actual_access:  read_only
        .address_space:  global
        .offset:         48
        .size:           8
        .value_kind:     global_buffer
      - .actual_access:  read_only
        .address_space:  global
        .offset:         56
        .size:           8
        .value_kind:     global_buffer
      - .actual_access:  read_only
        .address_space:  global
        .offset:         64
        .size:           8
        .value_kind:     global_buffer
      - .address_space:  global
        .offset:         72
        .size:           8
        .value_kind:     global_buffer
      - .actual_access:  read_only
        .address_space:  global
        .offset:         80
        .size:           8
        .value_kind:     global_buffer
      - .actual_access:  read_only
        .address_space:  global
        .offset:         88
        .size:           8
        .value_kind:     global_buffer
      - .actual_access:  read_only
        .address_space:  global
        .offset:         96
        .size:           8
        .value_kind:     global_buffer
      - .actual_access:  write_only
        .address_space:  global
        .offset:         104
        .size:           8
        .value_kind:     global_buffer
      - .address_space:  global
        .offset:         112
        .size:           8
        .value_kind:     global_buffer
      - .actual_access:  write_only
        .address_space:  global
        .offset:         120
        .size:           8
        .value_kind:     global_buffer
      - .actual_access:  write_only
        .address_space:  global
        .offset:         128
        .size:           8
        .value_kind:     global_buffer
      - .actual_access:  write_only
        .address_space:  global
        .offset:         136
        .size:           8
        .value_kind:     global_buffer
      - .actual_access:  write_only
        .address_space:  global
        .offset:         144
        .size:           8
        .value_kind:     global_buffer
    .group_segment_fixed_size: 30384
    .kernarg_segment_align: 8
    .kernarg_segment_size: 152
    .language:       OpenCL C
    .language_version:
      - 2
      - 0
    .max_flat_workgroup_size: 512
    .name:           _Z6k_iterILb1ELb0EEvPKfS1_PKiPK15HIP_vector_typeIfLj4EES7_S1_S1_S3_S1_PfS8_S1_S3_PDF16_PS5_SA_PiSA_SB_
    .private_segment_fixed_size: 0
    .sgpr_count:     102
    .sgpr_spill_count: 0
    .symbol:         _Z6k_iterILb1ELb0EEvPKfS1_PKiPK15HIP_vector_typeIfLj4EES7_S1_S1_S3_S1_PfS8_S1_S3_PDF16_PS5_SA_PiSA_SB_.kd
    .uniform_work_group_size: 1
    .uses_dynamic_stack: false
    .vgpr_count:     216
    .vgpr_spill_count: 0
    .wavefront_size: 64
  - .agpr_count:     0
    .args:
      - .actual_access:  read_only
        .address_space:  global
        .offset:         0
        .size:           8
        .value_kind:     global_buffer
      - .actual_access:  read_only
        .address_space:  global
        .offset:         8
        .size:           8
        .value_kind:     global_buffer
      - .actual_access:  read_only
        .address_space:  global
        .offset:         16
        .size:           8
        .value_kind:     global_buffer
      - .actual_access:  read_only
        .address_space:  global
        .offset:         24
        .size:           8
        .value_kind:     global_buffer
      - .actual_access:  read_only
        .address_space:  global
        .offset:         32
        .size:           8
        .value_kind:     global_buffer
      - .actual_access:  read_only
        .address_space:  global
        .offset:         40
        .size:           8
        .value_kind:     global_buffer
      - .actual_access:  read_only
        .address_space:  global
        .offset:         48
        .size:           8
        .value_kind:     global_buffer
      - .actual_access:  read_only
        .address_space:  global
        .offset:         56
        .size:           8
        .value_kind:     global_buffer
      - .actual_access:  read_only
        .address_space:  global
        .offset:         64
        .size:           8
        .value_kind:     global_buffer
      - .address_space:  global
        .offset:         72
        .size:           8
        .value_kind:     global_buffer
      - .actual_access:  read_only
        .address_space:  global
        .offset:         80
        .size:           8
        .value_kind:     global_buffer
      - .actual_access:  read_only
        .address_space:  global
        .offset:         88
        .size:           8
        .value_kind:     global_buffer
      - .actual_access:  read_only
        .address_space:  global
        .offset:         96
        .size:           8
        .value_kind:     global_buffer
      - .actual_access:  read_only
        .address_space:  global
        .offset:         104
        .size:           8
        .value_kind:     global_buffer
      - .actual_access:  read_only
        .address_space:  global
        .offset:         112
        .size:           8
        .value_kind:     global_buffer
      - .actual_access:  read_only
        .address_space:  global
        .offset:         120
        .size:           8
        .value_kind:     global_buffer
      - .actual_access:  read_only
        .address_space:  global
        .offset:         128
        .size:           8
        .value_kind:     global_buffer
      - .actual_access:  read_only
        .address_space:  global
        .offset:         136
        .size:           8
        .value_kind:     global_buffer
      - .actual_access:  read_only
        .address_space:  global
        .offset:         144
        .size:           8
        .value_kind:     global_buffer
    .group_segment_fixed_size: 5808
    .kernarg_segment_align: 8
    .kernarg_segment_size: 152
    .language:       OpenCL C
    .language_version:
      - 2
      - 0
    .max_flat_workgroup_size: 512
    .name:           _Z6k_iterILb0ELb0EEvPKfS1_PKiPK15HIP_vector_typeIfLj4EES7_S1_S1_S3_S1_PfS8_S1_S3_PDF16_PS5_SA_PiSA_SB_
    .private_segment_fixed_size: 0
    .sgpr_count:     46
    .sgpr_spill_count: 0
    .symbol:         _Z6k_iterILb0ELb0EEvPKfS1_PKiPK15HIP_vector_typeIfLj4EES7_S1_S1_S3_S1_PfS8_S1_S3_PDF16_PS5_SA_PiSA_SB_.kd
    .uniform_work_group_size: 1
    .uses_dynamic_stack: false
    .vgpr_count:     184
    .vgpr_spill_count: 0
    .wavefront_size: 64
  - .agpr_count:     0
    .args:
      - .actual_access:  read_only
        .address_space:  global
        .offset:         0
        .size:           8
        .value_kind:     global_buffer
      - .actual_access:  read_only
        .address_space:  global
        .offset:         8
        .size:           8
        .value_kind:     global_buffer
      - .actual_access:  read_only
        .address_space:  global
        .offset:         16
        .size:           8
        .value_kind:     global_buffer
      - .actual_access:  read_only
        .address_space:  global
        .offset:         24
        .size:           8
        .value_kind:     global_buffer
      - .actual_access:  read_only
        .address_space:  global
        .offset:         32
        .size:           8
        .value_kind:     global_buffer
      - .actual_access:  read_only
        .address_space:  global
        .offset:         40
        .size:           8
        .value_kind:     global_buffer
      - .actual_access:  read_only
        .address_space:  global
        .offset:         48
        .size:           8
        .value_kind:     global_buffer
      - .actual_access:  read_only
        .address_space:  global
        .offset:         56
        .size:           8
        .value_kind:     global_buffer
      - .actual_access:  read_only
        .address_space:  global
        .offset:         64
        .size:           8
        .value_kind:     global_buffer
      - .address_space:  global
        .offset:         72
        .size:           8
        .value_kind:     global_buffer
      - .actual_access:  write_only
        .address_space:  global
        .offset:         80
        .size:           8
        .value_kind:     global_buffer
      - .actual_access:  read_only
        .address_space:  global
        .offset:         88
        .size:           8
        .value_kind:     global_buffer
      - .actual_access:  read_only
        .address_space:  global
        .offset:         96
        .size:           8
        .value_kind:     global_buffer
      - .actual_access:  read_only
        .address_space:  global
        .offset:         104
        .size:           8
        .value_kind:     global_buffer
      - .actual_access:  read_only
        .address_space:  global
        .offset:         112
        .size:           8
        .value_kind:     global_buffer
      - .actual_access:  read_only
        .address_space:  global
        .offset:         120
        .size:           8
        .value_kind:     global_buffer
      - .actual_access:  read_only
        .address_space:  global
        .offset:         128
        .size:           8
        .value_kind:     global_buffer
      - .actual_access:  read_only
        .address_space:  global
        .offset:         136
        .size:           8
        .value_kind:     global_buffer
      - .actual_access:  read_only
        .address_space:  global
        .offset:         144
        .size:           8
        .value_kind:     global_buffer
    .group_segment_fixed_size: 5808
    .kernarg_segment_align: 8
    .kernarg_segment_size: 152
    .language:       OpenCL C
    .language_version:
      - 2
      - 0
    .max_flat_workgroup_size: 512
    .name:           _Z6k_iterILb0ELb1EEvPKfS1_PKiPK15HIP_vector_typeIfLj4EES7_S1_S1_S3_S1_PfS8_S1_S3_PDF16_PS5_SA_PiSA_SB_
    .private_segment_fixed_size: 0
    .sgpr_count:     46
    .sgpr_spill_count: 0
    .symbol:         _Z6k_iterILb0ELb1EEvPKfS1_PKiPK15HIP_vector_typeIfLj4EES7_S1_S1_S3_S1_PfS8_S1_S3_PDF16_PS5_SA_PiSA_SB_.kd
    .uniform_work_group_size: 1
    .uses_dynamic_stack: false
    .vgpr_count:     184
    .vgpr_spill_count: 0
    .wavefront_size: 64
